# MLA epilogue: out-projection results staged through per-wave LDS and written as coalesced 16-byte row stores
# speedup vs baseline: 1.0385x; 1.0125x over previous
.Lg_done:
	s_mov_b32 s99, 0
	v_ashrrev_i32_e32 v74, 4, v202
	v_lshlrev_b32_e32 v180, 4, v201
	v_ashrrev_i32_e32 v75, 31, v74
	v_lshl_add_u64 v[70:71], s[52:53], 0, v[180:181]
	v_lshlrev_b64 v[64:65], 8, v[74:75]
	v_lshl_add_u64 v[64:65], v[70:71], 0, v[64:65]
	global_load_dwordx4 v[64:67], v[64:65], off
	v_add_u32_e32 v204, 0x200, v202
	v_ashrrev_i32_e32 v76, 4, v204
	v_ashrrev_i32_e32 v77, 31, v76
	v_lshlrev_b64 v[204:205], 8, v[76:77]
	v_lshl_add_u64 v[204:205], v[70:71], 0, v[204:205]
	global_load_dwordx4 v[204:207], v[204:205], off
	v_add_u32_e32 v208, 0x400, v202
	v_ashrrev_i32_e32 v78, 4, v208
	v_ashrrev_i32_e32 v79, 31, v78
	v_lshlrev_b64 v[208:209], 8, v[78:79]
	v_lshl_add_u64 v[208:209], v[70:71], 0, v[208:209]
	global_load_dwordx4 v[208:211], v[208:209], off
	v_add_u32_e32 v212, 0x600, v202
	v_ashrrev_i32_e32 v80, 4, v212
	v_ashrrev_i32_e32 v81, 31, v80
	v_lshlrev_b64 v[212:213], 8, v[80:81]
	v_lshl_add_u64 v[212:213], v[70:71], 0, v[212:213]
	global_load_dwordx4 v[212:215], v[212:213], off
	s_mul_i32 s4, s67, 0xc00
	s_mul_hi_u32 s5, s66, 0xc00
	s_add_i32 s5, s5, s4
	s_mul_i32 s4, s66, 0xc00
	s_add_u32 s20, s80, s4
	v_add_u32_e32 v72, 0, v180
	s_addc_u32 s7, s81, s5
	v_mad_u64_u32 v[74:75], s[4:5], v74, s1, v[72:73]
	v_rcp_f32_e32 v68, v158
	s_and_b32 s21, s7, 0xffff
	s_and_b64 vcc, exec, s[62:63]
	v_readlane_b32 s62, v251, 12
	v_pk_mul_f32 v[48:49], v[68:69], v[48:49] op_sel_hi:[0,1]
	v_pk_mul_f32 v[32:33], v[68:69], v[32:33] op_sel_hi:[0,1]
	v_pk_mul_f32 v[0:1], v[68:69], v[0:1] op_sel_hi:[0,1]
	v_readlane_b32 s63, v251, 13
	s_waitcnt vmcnt(3)
	ds_write_b128 v74, v[64:67]
	v_mad_u64_u32 v[74:75], s[4:5], v76, s1, v[72:73]
	s_waitcnt vmcnt(2)
	ds_write_b128 v74, v[204:207]
	v_mad_u64_u32 v[74:75], s[4:5], v78, s1, v[72:73]
	s_waitcnt vmcnt(1)
	ds_write_b128 v74, v[208:211]
	v_mad_u64_u32 v[70:71], s[4:5], v80, s1, v[72:73]
	s_waitcnt vmcnt(0)
	ds_write_b128 v70, v[212:215]
	v_cvt_pk_bf16_f32 v64, v48, v49
	v_pk_mul_f32 v[48:49], v[68:69], v[50:51] op_sel_hi:[0,1]
	v_cvt_pk_bf16_f32 v65, v48, v49
	v_pk_mul_f32 v[48:49], v[68:69], v[52:53] op_sel_hi:[0,1]
	v_cvt_pk_bf16_f32 v66, v48, v49
	v_pk_mul_f32 v[48:49], v[68:69], v[54:55] op_sel_hi:[0,1]
	v_cvt_pk_bf16_f32 v52, v32, v33
	v_pk_mul_f32 v[32:33], v[68:69], v[34:35] op_sel_hi:[0,1]
	v_cvt_pk_bf16_f32 v67, v48, v49
	v_pk_mul_f32 v[48:49], v[68:69], v[56:57] op_sel_hi:[0,1]
	v_cvt_pk_bf16_f32 v53, v32, v33
	v_pk_mul_f32 v[32:33], v[68:69], v[36:37] op_sel_hi:[0,1]
	v_cvt_pk_bf16_f32 v56, v48, v49
	v_pk_mul_f32 v[48:49], v[68:69], v[58:59] op_sel_hi:[0,1]
	v_cvt_pk_bf16_f32 v54, v32, v33
	v_pk_mul_f32 v[32:33], v[68:69], v[38:39] op_sel_hi:[0,1]
	v_cvt_pk_bf16_f32 v57, v48, v49
	v_pk_mul_f32 v[48:49], v[68:69], v[60:61] op_sel_hi:[0,1]
	v_cvt_pk_bf16_f32 v55, v32, v33
	v_pk_mul_f32 v[32:33], v[68:69], v[40:41] op_sel_hi:[0,1]
	v_cvt_pk_bf16_f32 v40, v0, v1
	v_pk_mul_f32 v[0:1], v[68:69], v[2:3] op_sel_hi:[0,1]
	v_cvt_pk_bf16_f32 v58, v48, v49
	v_pk_mul_f32 v[48:49], v[68:69], v[62:63] op_sel_hi:[0,1]
	v_cvt_pk_bf16_f32 v41, v0, v1
	v_pk_mul_f32 v[0:1], v[68:69], v[4:5] op_sel_hi:[0,1]
	v_cvt_pk_bf16_f32 v59, v48, v49
	v_cvt_pk_bf16_f32 v48, v32, v33
	v_pk_mul_f32 v[32:33], v[68:69], v[42:43] op_sel_hi:[0,1]
	v_cvt_pk_bf16_f32 v42, v0, v1
	v_pk_mul_f32 v[0:1], v[68:69], v[6:7] op_sel_hi:[0,1]
	v_cvt_pk_bf16_f32 v43, v0, v1
	v_pk_mul_f32 v[0:1], v[68:69], v[8:9] op_sel_hi:[0,1]
	v_cvt_pk_bf16_f32 v36, v0, v1
	v_pk_mul_f32 v[0:1], v[68:69], v[10:11] op_sel_hi:[0,1]
	v_cvt_pk_bf16_f32 v37, v0, v1
	v_pk_mul_f32 v[0:1], v[68:69], v[12:13] op_sel_hi:[0,1]
	v_cvt_pk_bf16_f32 v49, v32, v33
	v_pk_mul_f32 v[32:33], v[68:69], v[44:45] op_sel_hi:[0,1]
	v_cvt_pk_bf16_f32 v38, v0, v1
	v_pk_mul_f32 v[0:1], v[68:69], v[14:15] op_sel_hi:[0,1]
	v_cvt_pk_bf16_f32 v50, v32, v33
	v_pk_mul_f32 v[32:33], v[68:69], v[46:47] op_sel_hi:[0,1]
	v_cvt_pk_bf16_f32 v39, v0, v1
	v_pk_mul_f32 v[0:1], v[68:69], v[16:17] op_sel_hi:[0,1]
	v_cvt_pk_bf16_f32 v51, v32, v33
	v_cvt_pk_bf16_f32 v32, v0, v1
	v_pk_mul_f32 v[0:1], v[68:69], v[18:19] op_sel_hi:[0,1]
	v_cvt_pk_bf16_f32 v33, v0, v1
	v_pk_mul_f32 v[0:1], v[68:69], v[20:21] op_sel_hi:[0,1]
	v_cvt_pk_bf16_f32 v34, v0, v1
	v_pk_mul_f32 v[0:1], v[68:69], v[22:23] op_sel_hi:[0,1]
	v_cvt_pk_bf16_f32 v35, v0, v1
	v_pk_mul_f32 v[0:1], v[68:69], v[24:25] op_sel_hi:[0,1]
	v_cvt_pk_bf16_f32 v16, v0, v1
	v_pk_mul_f32 v[0:1], v[68:69], v[26:27] op_sel_hi:[0,1]
	v_cvt_pk_bf16_f32 v17, v0, v1
	v_pk_mul_f32 v[0:1], v[68:69], v[28:29] op_sel_hi:[0,1]
	v_cvt_pk_bf16_f32 v18, v0, v1
	v_pk_mul_f32 v[0:1], v[68:69], v[30:31] op_sel_hi:[0,1]
	v_cvt_pk_bf16_f32 v19, v0, v1
	v_mul_u32_u24_e32 v0, 0x600, v200
	v_or_b32_e32 v20, v145, v0
	v_mul_u32_u24_e32 v0, 0x110, v200
	v_add3_u32 v21, 0, v169, v0
	s_waitcnt lgkmcnt(0)
	s_barrier
	v_lshlrev_b32_e32 v20, 1, v20
	v_add_u32_e32 v26, 0x2000, v21
	v_add_u32_e32 v27, 0x4000, v21
	v_add_u32_e32 v28, 0x6000, v21
	ds_read2_b64 v[76:79], v21 offset1:2
	ds_read2_b64 v[80:83], v21 offset0:4 offset1:6
	ds_read2_b64 v[84:87], v21 offset0:8 offset1:10
	ds_read2_b64 v[88:91], v21 offset0:12 offset1:14
	ds_read2_b64 v[92:95], v21 offset0:16 offset1:18
	ds_read2_b64 v[160:163], v21 offset0:20 offset1:22
	ds_read2_b64 v[164:167], v21 offset0:24 offset1:26
	ds_read2_b64 v[176:179], v21 offset0:28 offset1:30
	ds_read2_b64 v[204:207], v26 offset0:64 offset1:66
	ds_read2_b64 v[208:211], v26 offset0:68 offset1:70
	ds_read2_b64 v[212:215], v26 offset0:72 offset1:74
	ds_read2_b64 v[216:219], v26 offset0:76 offset1:78
	ds_read2_b64 v[220:223], v26 offset0:80 offset1:82
	ds_read2_b64 v[22:25], v26 offset0:84 offset1:86
	ds_read2_b64 v[68:71], v26 offset0:88 offset1:90
	ds_read2_b64 v[72:75], v26 offset0:92 offset1:94
	v_mbcnt_lo_u32_b32 v112, -1, 0
	v_mbcnt_hi_u32_b32 v112, -1, v112
	s_mul_i32 s98, s88, 9
	s_lshr_b32 s98, s98, 1
	s_add_i32 s98, s98, 0x9000
	v_and_b32_e32 v113, 31, v112
	v_lshrrev_b32_e32 v116, 5, v112
	v_mul_u32_u24_e32 v113, 0x90, v113
	v_lshl_add_u32 v113, v116, 3, v113
	v_add_u32_e32 v113, s98, v113
	v_lshrrev_b32_e32 v117, 3, v112
	v_and_b32_e32 v118, 7, v112
	v_mul_u32_u24_e32 v114, 0x90, v117
	v_lshl_add_u32 v114, v118, 4, v114
	v_add_u32_e32 v114, s98, v114
	v_mul_u32_u24_e32 v115, 0xc00, v117
	v_lshl_add_u32 v115, v118, 4, v115
	s_mov_b32 s32, 0x6000
	s_mov_b32 s98, 0xc000
	s_mov_b32 s100, 0x12000
	s_waitcnt lgkmcnt(8)
	v_mfma_f32_32x32x16_bf16 v[0:15], v[76:79], v[64:67], 0
	v_mfma_f32_32x32x16_bf16 v[0:15], v[80:83], v[56:59], v[0:15]
	v_mfma_f32_32x32x16_bf16 v[0:15], v[84:87], v[52:55], v[0:15]
	v_mfma_f32_32x32x16_bf16 v[0:15], v[88:91], v[48:51], v[0:15]
	v_mfma_f32_32x32x16_bf16 v[0:15], v[92:95], v[40:43], v[0:15]
	v_mfma_f32_32x32x16_bf16 v[0:15], v[160:163], v[36:39], v[0:15]
	v_mfma_f32_32x32x16_bf16 v[0:15], v[164:167], v[32:35], v[0:15]
	v_mfma_f32_32x32x16_bf16 v[0:15], v[176:179], v[16:19], v[0:15]
	ds_read2_b64 v[76:79], v27 offset0:128 offset1:130
	ds_read2_b64 v[80:83], v27 offset0:132 offset1:134
	ds_read2_b64 v[84:87], v27 offset0:136 offset1:138
	ds_read2_b64 v[88:91], v27 offset0:140 offset1:142
	ds_read2_b64 v[92:95], v27 offset0:144 offset1:146
	ds_read2_b64 v[160:163], v27 offset0:148 offset1:150
	ds_read2_b64 v[164:167], v27 offset0:152 offset1:154
	ds_read2_b64 v[176:179], v27 offset0:156 offset1:158
	s_nop 11
	v_cvt_pk_bf16_f32 v96, v0, v1
	v_cvt_pk_bf16_f32 v97, v2, v3
	ds_write_b64 v113, v[96:97] offset:0
	v_cvt_pk_bf16_f32 v98, v4, v5
	v_cvt_pk_bf16_f32 v99, v6, v7
	ds_write_b64 v113, v[98:99] offset:16
	v_cvt_pk_bf16_f32 v100, v8, v9
	v_cvt_pk_bf16_f32 v101, v10, v11
	ds_write_b64 v113, v[100:101] offset:32
	v_cvt_pk_bf16_f32 v102, v12, v13
	v_cvt_pk_bf16_f32 v103, v14, v15
	ds_write_b64 v113, v[102:103] offset:48
	s_waitcnt lgkmcnt(12)
	v_mfma_f32_32x32x16_bf16 v[0:15], v[204:207], v[64:67], 0
	v_mfma_f32_32x32x16_bf16 v[0:15], v[208:211], v[56:59], v[0:15]
	v_mfma_f32_32x32x16_bf16 v[0:15], v[212:215], v[52:55], v[0:15]
	v_mfma_f32_32x32x16_bf16 v[0:15], v[216:219], v[48:51], v[0:15]
	v_mfma_f32_32x32x16_bf16 v[0:15], v[220:223], v[40:43], v[0:15]
	v_mfma_f32_32x32x16_bf16 v[0:15], v[22:25], v[36:39], v[0:15]
	v_mfma_f32_32x32x16_bf16 v[0:15], v[68:71], v[32:35], v[0:15]
	v_mfma_f32_32x32x16_bf16 v[0:15], v[72:75], v[16:19], v[0:15]
	ds_read2_b64 v[204:207], v28 offset0:192 offset1:194
	ds_read2_b64 v[208:211], v28 offset0:196 offset1:198
	ds_read2_b64 v[212:215], v28 offset0:200 offset1:202
	ds_read2_b64 v[216:219], v28 offset0:204 offset1:206
	ds_read2_b64 v[220:223], v28 offset0:208 offset1:210
	ds_read2_b64 v[22:25], v28 offset0:212 offset1:214
	ds_read2_b64 v[68:71], v28 offset0:216 offset1:218
	ds_read2_b64 v[72:75], v28 offset0:220 offset1:222
	s_nop 11
	v_cvt_pk_bf16_f32 v96, v0, v1
	v_cvt_pk_bf16_f32 v97, v2, v3
	ds_write_b64 v113, v[96:97] offset:64
	v_cvt_pk_bf16_f32 v98, v4, v5
	v_cvt_pk_bf16_f32 v99, v6, v7
	ds_write_b64 v113, v[98:99] offset:80
	v_cvt_pk_bf16_f32 v100, v8, v9
	v_cvt_pk_bf16_f32 v101, v10, v11
	ds_write_b64 v113, v[100:101] offset:96
	v_cvt_pk_bf16_f32 v102, v12, v13
	v_cvt_pk_bf16_f32 v103, v14, v15
	ds_write_b64 v113, v[102:103] offset:112
	s_waitcnt lgkmcnt(0)
	ds_read_b128 v[116:119], v114
	ds_read_b128 v[120:123], v114 offset:1152
	ds_read_b128 v[124:127], v114 offset:2304
	ds_read_b128 v[128:131], v114 offset:3456
	v_mfma_f32_32x32x16_bf16 v[0:15], v[76:79], v[64:67], 0
	v_mfma_f32_32x32x16_bf16 v[0:15], v[80:83], v[56:59], v[0:15]
	v_mfma_f32_32x32x16_bf16 v[0:15], v[84:87], v[52:55], v[0:15]
	v_mfma_f32_32x32x16_bf16 v[0:15], v[88:91], v[48:51], v[0:15]
	v_mfma_f32_32x32x16_bf16 v[0:15], v[92:95], v[40:43], v[0:15]
	v_mfma_f32_32x32x16_bf16 v[0:15], v[160:163], v[36:39], v[0:15]
	v_mfma_f32_32x32x16_bf16 v[0:15], v[164:167], v[32:35], v[0:15]
	v_mfma_f32_32x32x16_bf16 v[0:15], v[176:179], v[16:19], v[0:15]
	s_waitcnt lgkmcnt(0)
	buffer_store_dwordx4 v[116:119], v115, s[20:23], 0 offen sc1
	buffer_store_dwordx4 v[120:123], v115, s[20:23], s32 offen sc1
	buffer_store_dwordx4 v[124:127], v115, s[20:23], s98 offen sc1
	buffer_store_dwordx4 v[128:131], v115, s[20:23], s100 offen sc1
	s_nop 11
	v_cvt_pk_bf16_f32 v96, v0, v1
	v_cvt_pk_bf16_f32 v97, v2, v3
	ds_write_b64 v113, v[96:97] offset:0
	v_cvt_pk_bf16_f32 v98, v4, v5
	v_cvt_pk_bf16_f32 v99, v6, v7
	ds_write_b64 v113, v[98:99] offset:16
	v_cvt_pk_bf16_f32 v100, v8, v9
	v_cvt_pk_bf16_f32 v101, v10, v11
	ds_write_b64 v113, v[100:101] offset:32
	v_cvt_pk_bf16_f32 v102, v12, v13
	v_cvt_pk_bf16_f32 v103, v14, v15
	ds_write_b64 v113, v[102:103] offset:48
	v_mfma_f32_32x32x16_bf16 v[0:15], v[204:207], v[64:67], 0
	v_mfma_f32_32x32x16_bf16 v[0:15], v[208:211], v[56:59], v[0:15]
	v_mfma_f32_32x32x16_bf16 v[0:15], v[212:215], v[52:55], v[0:15]
	v_mfma_f32_32x32x16_bf16 v[0:15], v[216:219], v[48:51], v[0:15]
	v_mfma_f32_32x32x16_bf16 v[0:15], v[220:223], v[40:43], v[0:15]
	v_mfma_f32_32x32x16_bf16 v[0:15], v[22:25], v[36:39], v[0:15]
	v_mfma_f32_32x32x16_bf16 v[0:15], v[68:71], v[32:35], v[0:15]
	v_mfma_f32_32x32x16_bf16 v[0:15], v[72:75], v[16:19], v[0:15]
	s_nop 11
	v_cvt_pk_bf16_f32 v96, v0, v1
	v_cvt_pk_bf16_f32 v97, v2, v3
	ds_write_b64 v113, v[96:97] offset:64
	v_cvt_pk_bf16_f32 v98, v4, v5
	v_cvt_pk_bf16_f32 v99, v6, v7
	ds_write_b64 v113, v[98:99] offset:80
	v_cvt_pk_bf16_f32 v100, v8, v9
	v_cvt_pk_bf16_f32 v101, v10, v11
	ds_write_b64 v113, v[100:101] offset:96
	v_cvt_pk_bf16_f32 v102, v12, v13
	v_cvt_pk_bf16_f32 v103, v14, v15
	ds_write_b64 v113, v[102:103] offset:112
	s_waitcnt lgkmcnt(0)
	ds_read_b128 v[116:119], v114
	ds_read_b128 v[120:123], v114 offset:1152
	ds_read_b128 v[124:127], v114 offset:2304
	ds_read_b128 v[128:131], v114 offset:3456
	s_waitcnt lgkmcnt(0)
	buffer_store_dwordx4 v[116:119], v115, s[20:23], 0 offen offset:128 sc1
	buffer_store_dwordx4 v[120:123], v115, s[20:23], s32 offen offset:128 sc1
	buffer_store_dwordx4 v[124:127], v115, s[20:23], s98 offen offset:128 sc1
	buffer_store_dwordx4 v[128:131], v115, s[20:23], s100 offen offset:128 sc1
	s_cbranch_vccz .LBB0_1339
	s_lshl_b32 s8, s8, 6
	s_ashr_i32 s9, s8, 31
	s_cmp_eq_u64 s[64:65], 0
	s_cbranch_scc1 .LBB0_1253
	s_lshl_b64 s[4:5], s[8:9], 2
	s_add_u32 s4, s64, s4
	s_addc_u32 s5, s65, s5
	v_lshlrev_b32_e32 v4, 2, v182
	global_load_dwordx4 v[0:3], v4, s[4:5] offset:16
	s_nop 0
	global_load_dwordx4 v[4:7], v4, s[4:5]
	s_branch .LBB0_1254
